# MoE phases: workgroup index rotated so the 32 workgroups of an XCD take 4 row tiles x 8 column tiles (A rows shared in that XCD's L2)
# speedup vs baseline: 1.0132x; 1.0124x over previous
; #define LAS __attribute__((address_space(3)))
;     template <class Tp> __device__ __forceinline__ Tp* w(size_t off) const { return (Tp*)(ws + off); }
; __device__ __forceinline__ void expert_offsets(const Frame& F, LAS int* offs, LAS int* cnts, LAS int* rt_exp) {
;     const int* cnt = F.w<int>(WS_CTL) + CW_CNT;
;     __syncthreads();
;     if (F.wave == 0) {
;         const int e = F.lane, cn = cnt[e * CNT_STRIDE], n = (cn + 255) >> 8;
;         int inc = n;
; #pragma unroll
;         for (int o = 1; o < 64; o <<= 1) { const int v = __shfl_up(inc, o); if (e >= o) inc += v; }
;         const int excl = inc - n;
;         cnts[e] = cn; offs[e] = excl * 256; if (e == 63) offs[64] = inc * 256;
;         for (int j = 0; j < n; ++j) rt_exp[excl + j] = e;
;     }
;     __syncthreads();
; }
; __device__ __forceinline__ void ph_moe1(const Frame& F) {
;     LAS int* offs = (LAS int*)(F.lds + LDS_TAB); LAS int* cnts = offs + 128; LAS int* rt_exp = offs + 256;
;     expert_offsets(F, offs, cnts, rt_exp);
;     pg8::GroupedOrder So; So.init(rt_exp, (offs[64] >> 8) * 8, (int)gridDim.x, (int)blockIdx.x);
.LBB0_1008:
	v_writelane_b32 v248, s97, 60
	s_and_b32 s0, s97, 7
	s_lshl_b32 s0, s0, 5
	s_lshr_b32 s1, s97, 3
	s_or_b32 s97, s0, s1
	s_cmp_lt_i32 s80, 8
	s_cselect_b64 s[0:1], -1, 0
	s_and_b64 s[0:1], s[0:1], s[2:3]
	s_andn2_b64 vcc, exec, s[0:1]
	s_cbranch_vccnz .LBB0_1147
	v_readlane_b32 s2, v248, 0
	v_readlane_b32 s3, v248, 1
	s_mov_b64 s[8:9], s[2:3]
	s_mov_b32 s24, s86
	s_load_dword s33, s[2:3], 0xd0
	s_load_dwordx4 s[4:7], s[8:9], 0x90
	s_nop 0
	s_load_dwordx2 s[2:3], s[8:9], 0xb8
	v_mbcnt_lo_u32_b32 v0, -1, 0
	s_mov_b32 s16, 0
	v_mbcnt_hi_u32_b32 v24, -1, v0
	s_cmp_lg_u32 s24, 0
	s_waitcnt vmcnt(0) lgkmcnt(0)
	s_barrier
	s_cbranch_scc1 .LBB0_1026
	v_lshlrev_b32_e32 v0, 8, v24
	v_mov_b32_e32 v1, 0
	v_lshl_add_u64 v[0:1], s[2:3], 0, v[0:1]
	v_add_co_u32_e32 v0, vcc, 0x40000, v0
	v_and_b32_e32 v2, 64, v24
	s_nop 0
	v_addc_co_u32_e32 v1, vcc, 0, v1, vcc
	global_load_dword v1, v[0:1], off
	v_add_u32_e32 v0, -1, v24
	v_cmp_lt_i32_e32 vcc, v0, v2
	v_add_u32_e32 v3, -2, v24
	v_add_u32_e32 v4, -4, v24
	v_cndmask_b32_e32 v0, v0, v24, vcc
	v_lshlrev_b32_e32 v9, 2, v0
	v_cmp_lt_i32_e32 vcc, v3, v2
	v_add_u32_e32 v5, -8, v24
	v_add_u32_e32 v6, -16, v24
	v_cndmask_b32_e32 v3, v3, v24, vcc
	v_cmp_lt_i32_e32 vcc, 0, v24
	v_lshlrev_b32_e32 v3, 2, v3
	v_subrev_u32_e32 v7, 32, v24
	v_lshl_add_u32 v8, v24, 2, 0
	s_waitcnt vmcnt(0)
	v_add_u32_e32 v0, 0xff, v1
	v_ashrrev_i32_e32 v0, 8, v0
	ds_bpermute_b32 v9, v9, v0
	s_waitcnt lgkmcnt(0)
	v_cndmask_b32_e32 v9, 0, v9, vcc
	v_add_u32_e32 v9, v0, v9
	ds_bpermute_b32 v3, v3, v9
	v_cmp_lt_i32_e32 vcc, v4, v2
	s_nop 1
	v_cndmask_b32_e32 v4, v4, v24, vcc
	v_cmp_lt_i32_e32 vcc, 1, v24
	v_lshlrev_b32_e32 v4, 2, v4
	s_waitcnt lgkmcnt(0)
	v_cndmask_b32_e32 v3, 0, v3, vcc
	v_add_u32_e32 v3, v9, v3
	ds_bpermute_b32 v4, v4, v3
	v_cmp_lt_i32_e32 vcc, v5, v2
	s_nop 1
	v_cndmask_b32_e32 v5, v5, v24, vcc
	v_cmp_lt_i32_e32 vcc, 3, v24
	v_lshlrev_b32_e32 v5, 2, v5
	s_waitcnt lgkmcnt(0)
	v_cndmask_b32_e32 v4, 0, v4, vcc
	v_add_u32_e32 v3, v3, v4
	ds_bpermute_b32 v4, v5, v3
	v_cmp_lt_i32_e32 vcc, v6, v2
	s_nop 1
	v_cndmask_b32_e32 v5, v6, v24, vcc
	v_cmp_lt_i32_e32 vcc, 7, v24
	v_lshlrev_b32_e32 v5, 2, v5
	s_waitcnt lgkmcnt(0)
	v_cndmask_b32_e32 v4, 0, v4, vcc
	v_add_u32_e32 v3, v3, v4
	ds_bpermute_b32 v4, v5, v3
	v_cmp_lt_i32_e32 vcc, v7, v2
	v_add_u32_e32 v5, 0x20000, v8
	s_nop 0
	v_cndmask_b32_e32 v2, v7, v24, vcc
	v_cmp_lt_i32_e32 vcc, 15, v24
	v_lshlrev_b32_e32 v2, 2, v2
	s_waitcnt lgkmcnt(0)
	v_cndmask_b32_e32 v4, 0, v4, vcc
	v_add_u32_e32 v3, v3, v4
	ds_bpermute_b32 v2, v2, v3
	v_add_u32_e32 v4, 0x20200, v8
	v_cmp_lt_i32_e32 vcc, 31, v24
	ds_write_b32 v4, v1
	s_waitcnt lgkmcnt(1)
	v_cndmask_b32_e32 v1, 0, v2, vcc
	v_add_u32_e32 v2, v3, v1
	v_sub_u32_e32 v1, v2, v0
	v_lshlrev_b32_e32 v3, 8, v1
	v_cmp_eq_u32_e32 vcc, 63, v24
	ds_write_b32 v5, v3
	s_and_saveexec_b64 s[8:9], vcc
	s_add_i32 s10, 0, 0x20100
	v_lshlrev_b32_e32 v2, 8, v2
	v_mov_b32_e32 v3, s10
	ds_write_b32 v3, v2
	s_or_b64 exec, exec, s[8:9]
	v_cmp_lt_i32_e32 vcc, 0, v0
	s_and_saveexec_b64 s[8:9], vcc
	s_cbranch_execz .LBB0_1025
	v_cmp_ne_u32_e32 vcc, 1, v0
	s_mov_b64 s[12:13], -1
	v_mov_b32_e32 v2, 0
	s_and_saveexec_b64 s[10:11], vcc
	s_cbranch_execz .LBB0_1022
	v_add_u32_e32 v3, -2, v0
	v_lshrrev_b32_e32 v2, 1, v3
	v_add_u32_e32 v2, 1, v2
	v_cmp_lt_u32_e32 vcc, 13, v3
	v_mov_b32_e32 v5, 0
	s_and_saveexec_b64 s[12:13], vcc
	s_cbranch_execz .LBB0_1018
	v_lshl_add_u32 v4, v1, 2, 0
	v_and_b32_e32 v3, -8, v2
	s_mov_b32 s17, 0
	v_add_u32_e32 v4, 0x20400, v4
	s_mov_b64 s[14:15], 0

;     template <class Tp> __device__ __forceinline__ Tp* w(size_t off) const { return (Tp*)(ws + off); }
; __device__ __forceinline__ void ph_final(const Frame& F) {
;     const bf16* X2 = F.w<bf16>(WS_X2); const bf16* Y2 = F.w<bf16>(WS_Y2); const float* gf = F.i_final_g;
;     u32x2 xa[8], ya[8], yb[8], xn[8], yan[8], ybn[8];
;     float4 gw[8];
; #pragma unroll
;     for (int j = 0; j < 8; ++j) gw[j] = ((const float4*)gf)[F.lane + 64 * j];
;     int m = F.gw;
;     if (m < T) { const u32x2* xr = (const u32x2*)(X2 + (size_t)m * D); const u32x2* y0 = (const u32x2*)(Y2 + (size_t)(2 * m) * D); const u32x2* y1 = (const u32x2*)(Y2 + (size_t)(2 * m + 1) * D);
; #pragma unroll
;         for (int j = 0; j < 8; ++j) { xa[j] = __builtin_nontemporal_load(xr + F.lane + 64 * j); ya[j] = __builtin_nontemporal_load(y0 + F.lane + 64 * j); yb[j] = __builtin_nontemporal_load(y1 + F.lane + 64 * j); } }
;     for (; m < T; m += F.NGW) {
;         const int mn = m + F.NGW;
;         if (mn < T) { const u32x2* xr = (const u32x2*)(X2 + (size_t)mn * D); const u32x2* y0 = (const u32x2*)(Y2 + (size_t)(2 * mn) * D); const u32x2* y1 = (const u32x2*)(Y2 + (size_t)(2 * mn + 1) * D);
; #pragma unroll
;             for (int j = 0; j < 8; ++j) { xn[j] = __builtin_nontemporal_load(xr + F.lane + 64 * j); yan[j] = __builtin_nontemporal_load(y0 + F.lane + 64 * j); ybn[j] = __builtin_nontemporal_load(y1 + F.lane + 64 * j); } }
.LBB0_1396:
	v_readlane_b32 s97, v248, 60
	s_cmp_lt_i32 s80, 10
	s_cselect_b64 s[0:1], -1, 0
	s_and_b64 s[0:1], s[0:1], s[2:3]
	s_andn2_b64 vcc, exec, s[0:1]
	s_cbranch_vccnz .LBB0_1402
	v_readlane_b32 s8, v248, 0
	v_readlane_b32 s9, v248, 1
	s_lshl_b32 s0, s97, 3
	s_add_i32 s4, s86, s0
	s_cmpk_gt_i32 s4, 0x3fff
	s_cbranch_scc1 .LBB0_1402
	v_readlane_b32 s0, v248, 0
	v_readlane_b32 s1, v248, 1
	s_load_dword s16, s[0:1], 0xd0
	s_load_dwordx2 s[10:11], s[8:9], 0xa8
	s_waitcnt vmcnt(0)
	v_mbcnt_lo_u32_b32 v0, -1, 0
	s_load_dwordx4 s[0:3], s[8:9], 0xb0
	v_mbcnt_hi_u32_b32 v40, -1, v0
	s_waitcnt lgkmcnt(0)
	s_lshl_b32 s6, s16, 3
	v_lshlrev_b32_e32 v34, 4, v40
	v_mov_b32_e32 v35, 0
	s_add_u32 s8, s2, 0xf000000
	s_addc_u32 s9, s3, 0
	s_ashr_i32 s5, s4, 31
	v_lshl_add_u64 v[16:17], s[10:11], 0, v[34:35]
	global_load_dwordx4 v[0:3], v34, s[10:11]
	global_load_dwordx4 v[4:7], v34, s[10:11] offset:1024
	global_load_dwordx4 v[8:11], v34, s[10:11] offset:2048
	global_load_dwordx4 v[12:15], v34, s[10:11] offset:3072
	s_lshl_b64 s[10:11], s[4:5], 12
	s_add_u32 s10, s2, s10
	s_addc_u32 s11, s3, s11
	s_lshl_b32 s12, s4, 1
	s_ashr_i32 s13, s12, 31
	s_lshl_b64 s[14:15], s[12:13], 12
	s_add_u32 s14, s8, s14
	v_add_co_u32_e32 v32, vcc, 0x1000, v16
	s_addc_u32 s15, s9, s15
	s_or_b32 s12, s12, 1
	v_addc_co_u32_e32 v33, vcc, 0, v17, vcc
	s_ashr_i32 s13, s12, 31
	v_lshlrev_b32_e32 v36, 3, v40
	v_mov_b32_e32 v37, v35
	global_load_dwordx4 v[16:19], v[32:33], off
	global_load_dwordx4 v[20:23], v[32:33], off offset:1024
	global_load_dwordx4 v[24:27], v[32:33], off offset:2048
	global_load_dwordx4 v[28:31], v[32:33], off offset:3072
	s_lshl_b64 s[12:13], s[12:13], 12
	v_lshl_add_u64 v[32:33], s[10:11], 0, v[36:37]
	s_mov_b64 s[10:11], 0x31000000
	s_mov_b32 s7, 0x31000000
	s_add_u32 s12, s8, s12
	v_lshl_add_u64 v[38:39], v[32:33], 0, s[10:11]
	v_add_co_u32_e32 v32, vcc, s7, v32
	s_addc_u32 s13, s9, s13
	s_nop 0
	v_addc_co_u32_e32 v33, vcc, 0, v33, vcc
	global_load_dwordx2 v[130:131], v36, s[14:15] nt
	global_load_dwordx2 v[124:125], v36, s[14:15] offset:512 nt
	global_load_dwordx2 v[118:119], v36, s[14:15] offset:1024 nt
	global_load_dwordx2 v[112:113], v36, s[14:15] offset:1536 nt
	global_load_dwordx2 v[128:129], v36, s[12:13] nt
	global_load_dwordx2 v[122:123], v36, s[12:13] offset:512 nt
	global_load_dwordx2 v[116:117], v36, s[12:13] offset:1024 nt
	global_load_dwordx2 v[106:107], v36, s[12:13] offset:1536 nt
	global_load_dwordx2 v[126:127], v[38:39], off offset:512 nt
	global_load_dwordx2 v[120:121], v[38:39], off offset:1024 nt
	global_load_dwordx2 v[114:115], v[38:39], off offset:1536 nt
	global_load_dwordx2 v[110:111], v[38:39], off offset:2048 nt
	global_load_dwordx2 v[132:133], v[32:33], off nt
	global_load_dwordx2 v[102:103], v[38:39], off offset:2560 nt
	global_load_dwordx2 v[96:97], v[38:39], off offset:3072 nt
	global_load_dwordx2 v[90:91], v[38:39], off offset:3584 nt
	global_load_dwordx2 v[108:109], v36, s[14:15] offset:2048 nt
	global_load_dwordx2 v[100:101], v36, s[14:15] offset:2560 nt
	global_load_dwordx2 v[94:95], v36, s[14:15] offset:3072 nt
	global_load_dwordx2 v[88:89], v36, s[14:15] offset:3584 nt
	global_load_dwordx2 v[104:105], v36, s[12:13] offset:2048 nt
	global_load_dwordx2 v[98:99], v36, s[12:13] offset:2560 nt
	global_load_dwordx2 v[92:93], v36, s[12:13] offset:3072 nt
	global_load_dwordx2 v[86:87], v36, s[12:13] offset:3584 nt
	v_and_b32_e32 v32, 64, v40
	v_add_u32_e32 v32, 64, v32
	v_xor_b32_e32 v33, 32, v40
	v_cmp_lt_i32_e32 vcc, v33, v32
	v_mov_b32_e32 v142, 0x358637bd
	s_nop 0
	v_cndmask_b32_e32 v33, v40, v33, vcc
	v_lshlrev_b32_e32 v136, 2, v33
	v_xor_b32_e32 v33, 16, v40
	v_cmp_lt_i32_e32 vcc, v33, v32
	s_nop 1
	v_cndmask_b32_e32 v33, v40, v33, vcc
	v_lshlrev_b32_e32 v137, 2, v33
	v_xor_b32_e32 v33, 8, v40
	v_cmp_lt_i32_e32 vcc, v33, v32
	s_nop 1
	v_cndmask_b32_e32 v33, v40, v33, vcc
	v_lshlrev_b32_e32 v138, 2, v33
	v_xor_b32_e32 v33, 4, v40
	v_cmp_lt_i32_e32 vcc, v33, v32
	s_nop 1
	v_cndmask_b32_e32 v33, v40, v33, vcc
	v_lshlrev_b32_e32 v139, 2, v33
	v_xor_b32_e32 v33, 2, v40
	v_cmp_lt_i32_e32 vcc, v33, v32
	s_nop 1
	v_cndmask_b32_e32 v33, v40, v33, vcc
	v_lshlrev_b32_e32 v140, 2, v33
	v_xor_b32_e32 v33, 1, v40
	v_cmp_lt_i32_e32 vcc, v33, v32
	s_nop 1
	v_cndmask_b32_e32 v32, v40, v33, vcc
	v_lshlrev_b32_e32 v141, 2, v32
	v_lshl_add_u64 v[32:33], s[8:9], 0, v[36:37]
	s_lshl_b64 s[8:9], s[4:5], 13
	s_add_u32 s0, s0, s8
	s_addc_u32 s1, s1, s9
	s_add_i32 s12, s4, s6
	v_lshl_add_u64 v[34:35], s[0:1], 0, v[34:35]
	s_mov_b64 s[0:1], 0x1000
	s_ashr_i32 s7, s6, 31
	s_ashr_i32 s13, s12, 31
	v_lshl_add_u64 v[34:35], v[34:35], 0, s[0:1]
	s_lshl_b64 s[0:1], s[6:7], 13
	s_lshl_b32 s8, s12, 1
	s_lshl_b32 s5, s16, 4
	s_lshl_b64 s[12:13], s[12:13], 12
	s_add_u32 s2, s2, s12
	s_addc_u32 s3, s3, s13
	v_lshl_add_u64 v[36:37], s[2:3], 0, v[36:37]
	v_lshl_add_u64 v[36:37], v[36:37], 0, s[10:11]
	s_lshl_b64 s[2:3], s[6:7], 12
	s_mov_b32 s7, 0x800000
	s_branch .LBB0_1400
